# speedup vs baseline: 1.0126x; 1.0003x over previous
.LBB0_28:
	s_sub_u32 s34, s2, 58
	s_cmp_lt_u32 s34, 8
	s_cbranch_scc0 .Lnerf_prep_nowarm
	s_getpc_b64 s[34:35]
	v_lshlrev_b32_e32 v62, 7, v0
	v_min_u32_e32 v62, 0x7700, v62
	s_add_u32 s34, s34, 0x880
	s_addc_u32 s35, s35, 0
	global_load_dword v63, v62, s[34:35]

	.amdhsa_kernel _Z9nerf_prepPKfS0_S0_S0_S0_S0_S0_S0_S0_S0_S0_PtPf
		.amdhsa_group_segment_fixed_size 0
		.amdhsa_private_segment_fixed_size 0
		.amdhsa_kernarg_size 104
		.amdhsa_user_sgpr_count 2
		.amdhsa_user_sgpr_dispatch_ptr 0
		.amdhsa_user_sgpr_queue_ptr 0
		.amdhsa_user_sgpr_kernarg_segment_ptr 1
		.amdhsa_user_sgpr_dispatch_id 0
		.amdhsa_user_sgpr_kernarg_preload_length 0
		.amdhsa_user_sgpr_kernarg_preload_offset 0
		.amdhsa_user_sgpr_private_segment_size 0
		.amdhsa_uses_dynamic_stack 0
		.amdhsa_enable_private_segment 0
		.amdhsa_system_sgpr_workgroup_id_x 1
		.amdhsa_system_sgpr_workgroup_id_y 0
		.amdhsa_system_sgpr_workgroup_id_z 0
		.amdhsa_system_sgpr_workgroup_info 0
		.amdhsa_system_vgpr_workitem_id 0
		.amdhsa_next_free_vgpr 64
		.amdhsa_next_free_sgpr 40
		.amdhsa_accum_offset 64
		.amdhsa_reserve_vcc 1
		.amdhsa_float_round_mode_32 0
		.amdhsa_float_round_mode_16_64 0
		.amdhsa_float_denorm_mode_32 3
		.amdhsa_float_denorm_mode_16_64 3
		.amdhsa_dx10_clamp 1
		.amdhsa_ieee_mode 1
		.amdhsa_fp16_overflow 0
		.amdhsa_tg_split 0
		.amdhsa_exception_fp_ieee_invalid_op 0
		.amdhsa_exception_fp_denorm_src 0
		.amdhsa_exception_fp_ieee_div_zero 0
		.amdhsa_exception_fp_ieee_overflow 0
		.amdhsa_exception_fp_ieee_underflow 0
		.amdhsa_exception_fp_ieee_inexact 0
		.amdhsa_exception_int_div_zero 0
	.end_amdhsa_kernel

amdhsa.kernels:
  - .agpr_count:     0
    .args:
      - .actual_access:  read_only
        .address_space:  global
        .offset:         0
        .size:           8
        .value_kind:     global_buffer
      - .actual_access:  read_only
        .address_space:  global
        .offset:         8
        .size:           8
        .value_kind:     global_buffer
      - .actual_access:  read_only
        .address_space:  global
        .offset:         16
        .size:           8
        .value_kind:     global_buffer
      - .actual_access:  read_only
        .address_space:  global
        .offset:         24
        .size:           8
        .value_kind:     global_buffer
      - .actual_access:  read_only
        .address_space:  global
        .offset:         32
        .size:           8
        .value_kind:     global_buffer
      - .actual_access:  read_only
        .address_space:  global
        .offset:         40
        .size:           8
        .value_kind:     global_buffer
      - .actual_access:  read_only
        .address_space:  global
        .offset:         48
        .size:           8
        .value_kind:     global_buffer
      - .actual_access:  read_only
        .address_space:  global
        .offset:         56
        .size:           8
        .value_kind:     global_buffer
      - .actual_access:  read_only
        .address_space:  global
        .offset:         64
        .size:           8
        .value_kind:     global_buffer
      - .actual_access:  read_only
        .address_space:  global
        .offset:         72
        .size:           8
        .value_kind:     global_buffer
      - .actual_access:  read_only
        .address_space:  global
        .offset:         80
        .size:           8
        .value_kind:     global_buffer
      - .actual_access:  write_only
        .address_space:  global
        .offset:         88
        .size:           8
        .value_kind:     global_buffer
      - .actual_access:  write_only
        .address_space:  global
        .offset:         96
        .size:           8
        .value_kind:     global_buffer
    .group_segment_fixed_size: 0
    .kernarg_segment_align: 8
    .kernarg_segment_size: 104
    .language:       OpenCL C
    .language_version:
      - 2
      - 0
    .max_flat_workgroup_size: 256
    .name:           _Z9nerf_prepPKfS0_S0_S0_S0_S0_S0_S0_S0_S0_S0_PtPf
    .private_segment_fixed_size: 0
    .sgpr_count:     46
    .sgpr_spill_count: 0
    .symbol:         _Z9nerf_prepPKfS0_S0_S0_S0_S0_S0_S0_S0_S0_S0_PtPf.kd
    .uniform_work_group_size: 1
    .uses_dynamic_stack: false
    .vgpr_count:     64
    .vgpr_spill_count: 0
    .wavefront_size: 64
  - .agpr_count:     0
    .args:
      - .actual_access:  read_only
        .address_space:  global
        .offset:         0
        .size:           8
        .value_kind:     global_buffer
      - .actual_access:  read_only
        .address_space:  global
        .offset:         8
        .size:           8
        .value_kind:     global_buffer
      - .actual_access:  read_only
        .address_space:  global
        .offset:         16
        .size:           8
        .value_kind:     global_buffer
      - .actual_access:  read_only
        .address_space:  global
        .offset:         24
        .size:           8
        .value_kind:     global_buffer
      - .actual_access:  read_only
        .address_space:  global
        .offset:         32
        .size:           8
        .value_kind:     global_buffer
      - .actual_access:  read_only
        .address_space:  global
        .offset:         40
        .size:           8
        .value_kind:     global_buffer
      - .actual_access:  read_only
        .address_space:  global
        .offset:         48
        .size:           8
        .value_kind:     global_buffer
      - .actual_access:  write_only
        .address_space:  global
        .offset:         56
        .size:           8
        .value_kind:     global_buffer
    .group_segment_fixed_size: 147456
    .kernarg_segment_align: 8
    .kernarg_segment_size: 64
    .language:       OpenCL C
    .language_version:
      - 2
      - 0
    .max_flat_workgroup_size: 512
    .name:           _Z9nerf_mainPKfS0_S0_PKiS2_PKcS0_Pf
    .private_segment_fixed_size: 0
    .sgpr_count:     55
    .sgpr_spill_count: 0
    .symbol:         _Z9nerf_mainPKfS0_S0_PKiS2_PKcS0_Pf.kd
    .uniform_work_group_size: 1
    .uses_dynamic_stack: false
    .vgpr_count:     256
    .vgpr_spill_count: 0
    .wavefront_size: 64
